# baseline (speedup 1.0000x reference)
.LBB3_33:
	s_waitcnt lgkmcnt(0)
	s_barrier
	s_add_i32 s60, s45, 16
	s_and_b32 s60, s60, 28
	s_or_b32 s60, s60, 2
	s_lshl_b32 s60, s60, 15
	s_or_b32 s61, s60, 0x4000
	s_mov_b32 m0, s38
	s_nop 0
	buffer_load_dwordx4 v166, s[12:15], s61 offen lds
	s_or_b32 s61, s60, 0x6000
	s_mov_b32 m0, s39
	s_nop 0
	buffer_load_dwordx4 v166, s[12:15], s61 offen lds
	s_or_b32 s61, s60, 0xc000
	s_mov_b32 m0, s40
	s_nop 0
	buffer_load_dwordx4 v166, s[12:15], s61 offen lds
	s_or_b32 s61, s60, 0xe000
	s_mov_b32 m0, s42
	s_nop 0
	buffer_load_dwordx4 v166, s[12:15], s61 offen lds
	s_lshr_b32 s62, s21, 1
	s_lshr_b32 s63, s20, 2
	s_xor_b32 s62, s62, s63
	s_and_b32 s62, s62, 1
	s_lshl_b32 s63, s62, 16
	v_add_u32_e32 v232, s63, v168
	v_add_u32_e32 v233, 0x8000, v232
	s_add_i32 s63, s45, 16
	s_and_b32 s63, s63, 28
	s_lshl_b32 s64, s62, 1
	s_or_b32 s63, s63, s64
	s_add_i32 s63, s63, s41
	s_lshl_b32 s63, s63, 1
	v_mov_b32_e32 v234, s63
	s_or_b32 s63, s63, 1
	v_mov_b32_e32 v235, s63
	s_lshl_b32 s64, s62, 8
	s_add_i32 s64, s64, s47
	s_add_i32 s64, s64, 0x20600
	v_lshl_add_u32 v236, v167, 2, s64
	s_waitcnt vmcnt(4)
	s_barrier
	s_movk_i32 s65, 0xffc0
	s_movk_i32 s66, 0xff80
	s_brev_b32 s67, -2
	s_add_i32 s68, s45, 12
	s_and_b32 s68, s68, 28
	s_or_b32 s68, s68, 2
	s_add_i32 s68, s68, s41
	s_lshl_b32 s68, s68, 1
	v_mov_b32_e32 v176, s68
	s_or_b32 s68, s68, 1
	v_mov_b32_e32 v177, s68
	s_add_i32 s68, s47, 0x20500
	v_lshl_add_u32 v182, v167, 2, s68
	ds_read_b128 v[144:147], v232 offset:0
	ds_read_b128 v[148:151], v232 offset:256
	ds_read_b128 v[152:155], v232 offset:2048
	ds_read_b128 v[156:159], v232 offset:2304
	ds_read_b128 v[224:227], v232 offset:4096
	s_waitcnt lgkmcnt(4)
	v_mfma_f32_16x16x32_bf16 v[208:211], v[0:3], v[144:147], 0
	v_mfma_f32_16x16x32_bf16 v[212:215], v[4:7], v[144:147], 0
	ds_read_b128 v[228:231], v232 offset:4352
	s_waitcnt lgkmcnt(4)
	v_mfma_f32_16x16x32_bf16 v[216:219], v[0:3], v[148:151], 0
	v_mfma_f32_16x16x32_bf16 v[220:223], v[4:7], v[148:151], 0
	ds_read_b128 v[144:147], v232 offset:6144
	s_waitcnt lgkmcnt(4)
	v_mfma_f32_16x16x32_bf16 v[208:211], v[8:11], v[152:155], v[208:211]
	v_mfma_f32_16x16x32_bf16 v[212:215], v[12:15], v[152:155], v[212:215]
	ds_read_b128 v[148:151], v232 offset:6400
	v_and_or_b32 v180, v136, s65, v176
	v_and_or_b32 v181, v140, s65, v177
	v_max3_f32 v161, v161, v180, v181
	v_and_b32_e32 v178, 0xffffff80, v136
	v_and_b32_e32 v179, 0xffffff80, v140
	s_waitcnt lgkmcnt(4)
	v_mfma_f32_16x16x32_bf16 v[216:219], v[8:11], v[156:159], v[216:219]
	v_mfma_f32_16x16x32_bf16 v[220:223], v[12:15], v[156:159], v[220:223]
	ds_read_b128 v[152:155], v232 offset:8192
	v_and_or_b32 v180, v137, s65, v176
	v_and_or_b32 v181, v141, s65, v177
	v_max3_f32 v160, v160, v180, v181
	v_and_or_b32 v180, v137, s66, 1
	v_and_or_b32 v181, v141, s66, 1
	v_max_f32_e32 v178, v178, v180
	v_max_f32_e32 v179, v179, v181
	s_waitcnt lgkmcnt(4)
	v_mfma_f32_16x16x32_bf16 v[208:211], v[16:19], v[224:227], v[208:211]
	v_mfma_f32_16x16x32_bf16 v[212:215], v[20:23], v[224:227], v[212:215]
	ds_read_b128 v[156:159], v232 offset:8448
	v_and_or_b32 v180, v138, s65, v176
	v_and_or_b32 v181, v142, s65, v177
	v_max3_f32 v162, v162, v180, v181
	v_and_or_b32 v180, v138, s66, 2
	v_and_or_b32 v181, v142, s66, 2
	v_max_f32_e32 v178, v178, v180
	v_max_f32_e32 v179, v179, v181
	s_waitcnt lgkmcnt(4)
	v_mfma_f32_16x16x32_bf16 v[216:219], v[16:19], v[228:231], v[216:219]
	v_mfma_f32_16x16x32_bf16 v[220:223], v[20:23], v[228:231], v[220:223]
	ds_read_b128 v[224:227], v232 offset:10240
	v_and_or_b32 v180, v139, s65, v176
	v_and_or_b32 v181, v143, s65, v177
	v_max3_f32 v163, v163, v180, v181
	v_and_or_b32 v180, v139, s66, 3
	v_and_or_b32 v181, v143, s66, 3
	v_max_f32_e32 v178, v178, v180
	v_max_f32_e32 v179, v179, v181
	s_waitcnt lgkmcnt(4)
	v_mfma_f32_16x16x32_bf16 v[208:211], v[24:27], v[144:147], v[208:211]
	v_mfma_f32_16x16x32_bf16 v[212:215], v[28:31], v[144:147], v[212:215]
	ds_read_b128 v[228:231], v232 offset:10496
	v_and_or_b32 v180, v128, s65, v176
	v_and_or_b32 v181, v132, s65, v177
	v_max3_f32 v203, v203, v180, v181
	v_and_or_b32 v180, v128, s66, 4
	v_and_or_b32 v181, v132, s66, 4
	v_max_f32_e32 v178, v178, v180
	v_max_f32_e32 v179, v179, v181
	s_waitcnt lgkmcnt(4)
	v_mfma_f32_16x16x32_bf16 v[216:219], v[24:27], v[148:151], v[216:219]
	v_mfma_f32_16x16x32_bf16 v[220:223], v[28:31], v[148:151], v[220:223]
	ds_read_b128 v[144:147], v232 offset:12288
	v_and_or_b32 v180, v129, s65, v176
	v_and_or_b32 v181, v133, s65, v177
	v_max3_f32 v204, v204, v180, v181
	v_and_or_b32 v180, v129, s66, 5
	v_and_or_b32 v181, v133, s66, 5
	v_max_f32_e32 v178, v178, v180
	v_max_f32_e32 v179, v179, v181
	s_waitcnt lgkmcnt(4)
	v_mfma_f32_16x16x32_bf16 v[208:211], v[32:35], v[152:155], v[208:211]
	v_mfma_f32_16x16x32_bf16 v[212:215], v[36:39], v[152:155], v[212:215]
	ds_read_b128 v[148:151], v232 offset:12544
	v_and_or_b32 v180, v130, s65, v176
	v_and_or_b32 v181, v134, s65, v177
	v_max3_f32 v205, v205, v180, v181
	v_and_or_b32 v180, v130, s66, 6
	v_and_or_b32 v181, v134, s66, 6
	v_max_f32_e32 v178, v178, v180
	v_max_f32_e32 v179, v179, v181
	s_waitcnt lgkmcnt(4)
	v_mfma_f32_16x16x32_bf16 v[216:219], v[32:35], v[156:159], v[216:219]
	v_mfma_f32_16x16x32_bf16 v[220:223], v[36:39], v[156:159], v[220:223]
	ds_read_b128 v[152:155], v232 offset:14336
	v_and_or_b32 v180, v131, s65, v176
	v_and_or_b32 v181, v135, s65, v177
	v_max3_f32 v206, v206, v180, v181
	v_and_or_b32 v180, v131, s66, 7
	v_and_or_b32 v181, v135, s66, 7
	v_max_f32_e32 v178, v178, v180
	v_max_f32_e32 v179, v179, v181
	s_waitcnt lgkmcnt(4)
	v_mfma_f32_16x16x32_bf16 v[208:211], v[40:43], v[224:227], v[208:211]
	v_mfma_f32_16x16x32_bf16 v[212:215], v[44:47], v[224:227], v[212:215]
	ds_read_b128 v[156:159], v232 offset:14592
	v_or_b32_e32 v183, v173, v178
	v_ashrrev_i32_e32 v180, 31, v178
	v_bitop3_b32 v183, v180, v183, s67 bitop3:0x6c
	v_or_b32_e32 v184, v173, v179
	v_ashrrev_i32_e32 v181, 31, v179
	v_bitop3_b32 v184, v181, v184, s67 bitop3:0x6c
	s_waitcnt lgkmcnt(4)
	v_mfma_f32_16x16x32_bf16 v[216:219], v[40:43], v[228:231], v[216:219]
	v_mfma_f32_16x16x32_bf16 v[220:223], v[44:47], v[228:231], v[220:223]
	s_waitcnt lgkmcnt(3)
	v_mfma_f32_16x16x32_bf16 v[208:211], v[48:51], v[144:147], v[208:211]
	v_mfma_f32_16x16x32_bf16 v[212:215], v[52:55], v[144:147], v[212:215]
	s_waitcnt lgkmcnt(2)
	v_mfma_f32_16x16x32_bf16 v[216:219], v[48:51], v[148:151], v[216:219]
	v_mfma_f32_16x16x32_bf16 v[220:223], v[52:55], v[148:151], v[220:223]
	s_waitcnt lgkmcnt(1)
	v_mfma_f32_16x16x32_bf16 v[208:211], v[56:59], v[152:155], v[208:211]
	v_mfma_f32_16x16x32_bf16 v[212:215], v[60:63], v[152:155], v[212:215]
	s_waitcnt lgkmcnt(0)
	v_mfma_f32_16x16x32_bf16 v[216:219], v[56:59], v[156:159], v[216:219]
	v_mfma_f32_16x16x32_bf16 v[220:223], v[60:63], v[156:159], v[220:223]
	s_waitcnt vmcnt(0)
	s_barrier
	ds_read_b128 v[144:147], v233 offset:0
	ds_read_b128 v[148:151], v233 offset:256
	ds_read_b128 v[152:155], v233 offset:2048
	ds_read_b128 v[156:159], v233 offset:2304
	ds_read_b128 v[224:227], v233 offset:4096
	s_waitcnt lgkmcnt(4)
	v_mfma_f32_16x16x32_bf16 v[208:211], v[64:67], v[144:147], v[208:211]
	v_mfma_f32_16x16x32_bf16 v[212:215], v[68:71], v[144:147], v[212:215]
	ds_read_b128 v[228:231], v233 offset:4352
	s_waitcnt lgkmcnt(4)
	v_mfma_f32_16x16x32_bf16 v[216:219], v[64:67], v[148:151], v[216:219]
	v_mfma_f32_16x16x32_bf16 v[220:223], v[68:71], v[148:151], v[220:223]
	ds_read_b128 v[144:147], v233 offset:6144
	s_waitcnt lgkmcnt(4)
	v_mfma_f32_16x16x32_bf16 v[208:211], v[72:75], v[152:155], v[208:211]
	v_mfma_f32_16x16x32_bf16 v[212:215], v[76:79], v[152:155], v[212:215]
	ds_read_b128 v[148:151], v233 offset:6400
	s_waitcnt lgkmcnt(4)
	v_mfma_f32_16x16x32_bf16 v[216:219], v[72:75], v[156:159], v[216:219]
	v_mfma_f32_16x16x32_bf16 v[220:223], v[76:79], v[156:159], v[220:223]
	ds_read_b128 v[152:155], v233 offset:8192
	s_waitcnt lgkmcnt(4)
	v_mfma_f32_16x16x32_bf16 v[208:211], v[80:83], v[224:227], v[208:211]
	v_mfma_f32_16x16x32_bf16 v[212:215], v[84:87], v[224:227], v[212:215]
	ds_read_b128 v[156:159], v233 offset:8448
	s_waitcnt lgkmcnt(4)
	v_mfma_f32_16x16x32_bf16 v[216:219], v[80:83], v[228:231], v[216:219]
	v_mfma_f32_16x16x32_bf16 v[220:223], v[84:87], v[228:231], v[220:223]
	ds_read_b128 v[224:227], v233 offset:10240
	s_waitcnt lgkmcnt(4)
	v_mfma_f32_16x16x32_bf16 v[208:211], v[88:91], v[144:147], v[208:211]
	v_mfma_f32_16x16x32_bf16 v[212:215], v[92:95], v[144:147], v[212:215]
	ds_read_b128 v[228:231], v233 offset:10496
	s_waitcnt lgkmcnt(4)
	v_mfma_f32_16x16x32_bf16 v[216:219], v[88:91], v[148:151], v[216:219]
	v_mfma_f32_16x16x32_bf16 v[220:223], v[92:95], v[148:151], v[220:223]
	ds_read_b128 v[144:147], v233 offset:12288
	s_waitcnt lgkmcnt(4)
	v_mfma_f32_16x16x32_bf16 v[208:211], v[96:99], v[152:155], v[208:211]
	v_mfma_f32_16x16x32_bf16 v[212:215], v[100:103], v[152:155], v[212:215]
	ds_read_b128 v[148:151], v233 offset:12544
	s_waitcnt lgkmcnt(4)
	v_mfma_f32_16x16x32_bf16 v[216:219], v[96:99], v[156:159], v[216:219]
	v_mfma_f32_16x16x32_bf16 v[220:223], v[100:103], v[156:159], v[220:223]
	ds_read_b128 v[152:155], v233 offset:14336
	s_waitcnt lgkmcnt(4)
	v_mfma_f32_16x16x32_bf16 v[208:211], v[104:107], v[224:227], v[208:211]
	v_mfma_f32_16x16x32_bf16 v[212:215], v[108:111], v[224:227], v[212:215]
	ds_read_b128 v[156:159], v233 offset:14592
	s_waitcnt lgkmcnt(4)
	v_mfma_f32_16x16x32_bf16 v[216:219], v[104:107], v[228:231], v[216:219]
	v_mfma_f32_16x16x32_bf16 v[220:223], v[108:111], v[228:231], v[220:223]
	s_waitcnt lgkmcnt(3)
	v_mfma_f32_16x16x32_bf16 v[208:211], v[112:115], v[144:147], v[208:211]
	v_mfma_f32_16x16x32_bf16 v[212:215], v[116:119], v[144:147], v[212:215]
	s_waitcnt lgkmcnt(2)
	v_mfma_f32_16x16x32_bf16 v[216:219], v[112:115], v[148:151], v[216:219]
	v_mfma_f32_16x16x32_bf16 v[220:223], v[116:119], v[148:151], v[220:223]
	s_waitcnt lgkmcnt(1)
	v_mfma_f32_16x16x32_bf16 v[208:211], v[120:123], v[152:155], v[208:211]
	v_mfma_f32_16x16x32_bf16 v[212:215], v[124:127], v[152:155], v[212:215]
	s_waitcnt lgkmcnt(0)
	v_mfma_f32_16x16x32_bf16 v[216:219], v[120:123], v[156:159], v[216:219]
	v_mfma_f32_16x16x32_bf16 v[220:223], v[124:127], v[156:159], v[220:223]
	s_nop 7
	s_nop 3
	v_and_or_b32 v237, v208, s65, v234
	v_and_or_b32 v238, v216, s65, v235
	v_max3_f32 v161, v161, v237, v238
	v_and_b32_e32 v174, 0xffffff80, v208
	v_and_b32_e32 v175, 0xffffff80, v216
	v_and_or_b32 v237, v209, s65, v234
	v_and_or_b32 v238, v217, s65, v235
	v_max3_f32 v160, v160, v237, v238
	v_and_or_b32 v237, v209, s66, 1
	v_and_or_b32 v238, v217, s66, 1
	v_max_f32_e32 v174, v174, v237
	v_max_f32_e32 v175, v175, v238
	v_and_or_b32 v237, v210, s65, v234
	v_and_or_b32 v238, v218, s65, v235
	v_max3_f32 v162, v162, v237, v238
	v_and_or_b32 v237, v210, s66, 2
	v_and_or_b32 v238, v218, s66, 2
	v_max_f32_e32 v174, v174, v237
	v_max_f32_e32 v175, v175, v238
	v_and_or_b32 v237, v211, s65, v234
	v_and_or_b32 v238, v219, s65, v235
	v_max3_f32 v163, v163, v237, v238
	v_and_or_b32 v237, v211, s66, 3
	v_and_or_b32 v238, v219, s66, 3
	v_max_f32_e32 v174, v174, v237
	v_max_f32_e32 v175, v175, v238
	v_and_or_b32 v237, v212, s65, v234
	v_and_or_b32 v238, v220, s65, v235
	v_max3_f32 v203, v203, v237, v238
	v_and_or_b32 v237, v212, s66, 4
	v_and_or_b32 v238, v220, s66, 4
	v_max_f32_e32 v174, v174, v237
	v_max_f32_e32 v175, v175, v238
	v_and_or_b32 v237, v213, s65, v234
	v_and_or_b32 v238, v221, s65, v235
	v_max3_f32 v204, v204, v237, v238
	v_and_or_b32 v237, v213, s66, 5
	v_and_or_b32 v238, v221, s66, 5
	v_max_f32_e32 v174, v174, v237
	v_max_f32_e32 v175, v175, v238
	v_and_or_b32 v237, v214, s65, v234
	v_and_or_b32 v238, v222, s65, v235
	v_max3_f32 v205, v205, v237, v238
	v_and_or_b32 v237, v214, s66, 6
	v_and_or_b32 v238, v222, s66, 6
	v_max_f32_e32 v174, v174, v237
	v_max_f32_e32 v175, v175, v238
	v_and_or_b32 v237, v215, s65, v234
	v_and_or_b32 v238, v223, s65, v235
	v_max3_f32 v206, v206, v237, v238
	v_and_or_b32 v237, v215, s66, 7
	v_and_or_b32 v238, v223, s66, 7
	v_max_f32_e32 v174, v174, v237
	v_max_f32_e32 v175, v175, v238
	v_or_b32_e32 v237, v173, v174
	v_ashrrev_i32_e32 v238, 31, v174
	v_bitop3_b32 v237, v238, v237, s67 bitop3:0x6c
	ds_max_i32 v236, v237
	v_or_b32_e32 v237, v173, v175
	v_ashrrev_i32_e32 v238, 31, v175
	v_bitop3_b32 v237, v238, v237, s67 bitop3:0x6c
	ds_max_i32 v236, v237 offset:64
	ds_max_i32 v182, v183
	ds_max_i32 v182, v184 offset:64
	v_mov_b32_e32 v0, v161
	v_mov_b32_e32 v1, v160
	v_mov_b32_e32 v3, v162
	v_mov_b32_e32 v4, v163
	v_mov_b32_e32 v5, v203
	v_mov_b32_e32 v6, v204
	v_mov_b32_e32 v7, v205
	v_mov_b32_e32 v8, v206
	v_mbcnt_lo_u32_b32 v2, -1, 0
	s_lshl_b64 s[0:1], s[16:17], 13
	s_waitcnt vmcnt(0)
	v_mbcnt_hi_u32_b32 v2, -1, v2
	s_add_u32 s4, s10, s0
	s_addc_u32 s5, s11, s1
	s_lshl_b32 s0, s21, 12
	v_lshl_or_b32 v9, v2, 2, s0
	ds_write2st64_b32 v9, v0, v1 offset1:1
	ds_write2st64_b32 v9, v3, v4 offset0:2 offset1:3
	ds_write2st64_b32 v9, v5, v6 offset0:4 offset1:5
	ds_write2st64_b32 v9, v7, v8 offset0:6 offset1:7
	v_lshl_or_b32 v0, v2, 5, s0
	ds_read_b128 v[4:7], v0
	ds_read_b128 v[8:11], v0 offset:16
	s_movk_i32 s0, 0x3f0
	s_waitcnt lgkmcnt(1)
	v_cmp_gt_f32_e32 vcc, v5, v4
	s_nop 1
	v_cndmask_b32_e32 v1, v4, v5, vcc
	v_cndmask_b32_e64 v0, 0, 1, vcc
	v_cmp_gt_f32_e32 vcc, v6, v1
	v_and_b32_e32 v5, 1, v2
	v_lshlrev_b32_e32 v4, 3, v5
	v_cndmask_b32_e32 v1, v1, v6, vcc
	v_cndmask_b32_e64 v0, v0, 2, vcc
	v_cmp_gt_f32_e32 vcc, v7, v1
	s_nop 1
	v_cndmask_b32_e32 v1, v1, v7, vcc
	v_cndmask_b32_e64 v0, v0, 3, vcc
	s_waitcnt lgkmcnt(0)
	v_cmp_gt_f32_e32 vcc, v8, v1
	s_nop 1
	v_cndmask_b32_e32 v1, v1, v8, vcc
	v_cndmask_b32_e64 v0, v0, 4, vcc
	v_cmp_gt_f32_e32 vcc, v9, v1
	s_nop 1
	v_cndmask_b32_e32 v1, v1, v9, vcc
	v_cndmask_b32_e64 v0, v0, 5, vcc
	v_cmp_gt_f32_e32 vcc, v10, v1
	s_nop 1
	v_cndmask_b32_e32 v1, v1, v10, vcc
	v_cndmask_b32_e64 v0, v0, 6, vcc
	v_cmp_gt_f32_e32 vcc, v11, v1
	s_nop 1
	v_cndmask_b32_e32 v1, v1, v11, vcc
	v_cndmask_b32_e64 v3, v0, 7, vcc
	v_and_b32_e32 v0, 0xffffffc0, v1
	v_lshlrev_b32_e32 v1, 4, v1
	v_and_or_b32 v1, v1, s0, v4
	v_add_u32_e32 v1, v1, v3
	s_nop 1
	v_mov_b32_dpp v3, v0 quad_perm:[1,0,3,2] row_mask:0xf bank_mask:0xf
	v_mov_b32_dpp v4, v1 quad_perm:[1,0,3,2] row_mask:0xf bank_mask:0xf
	v_cmp_eq_u32_e32 vcc, 0, v5
	s_and_saveexec_b64 s[0:1], vcc
	s_cbranch_execz .LBB3_37
	s_waitcnt lgkmcnt(1)
	v_cmp_eq_f32_e64 s[0:1], v3, v0
	s_waitcnt lgkmcnt(0)
	v_cmp_lt_i32_e64 s[2:3], v4, v1
	v_cmp_gt_f32_e32 vcc, v3, v0
	s_and_b64 s[0:1], s[0:1], s[2:3]
	s_or_b64 vcc, vcc, s[0:1]
	v_lshlrev_b32_e32 v5, 1, v2
	v_cndmask_b32_e32 v4, v1, v4, vcc
	v_lshrrev_b32_e32 v1, 1, v2
	v_and_b32_e32 v5, 12, v5
	v_cndmask_b32_e32 v0, v0, v3, vcc
	v_and_or_b32 v5, v1, 48, v5
	v_bfe_u32 v2, v2, 3, 2
	v_bfrev_b32_e32 v1, 1
	v_cmp_lt_i32_e32 vcc, -1, v0
	v_lshl_or_b32 v2, s20, 7, v2
	v_or_b32_e32 v2, s46, v2
	v_cndmask_b32_e32 v1, -1, v1, vcc
	v_xor_b32_e32 v1, v1, v0
	v_sub_u32_e32 v0, 0, v4
	v_add_u32_e32 v0, 0x3ff, v0
	v_add_lshl_u32 v2, v2, v5, 3
	global_atomic_umax_x2 v2, v[0:1], s[4:5]
.LBB3_37:
	s_mov_b64 exec, -1
	v_mbcnt_lo_u32_b32 v2, -1, 0
	v_mbcnt_hi_u32_b32 v2, -1, v2
	s_andn2_b32 s23, s23, 63
	v_add_u32_e32 v9, s23, v2
	s_movk_i32 s2, 0xff80
	s_brev_b32 s3, -2
	s_waitcnt lgkmcnt(0)
	s_barrier
	v_mov_b32_e32 v10, 0x20000
	v_lshl_add_u32 v10, v9, 2, v10
	ds_read_b32 v10, v10
	s_movk_i32 s6, 0x63
	v_and_b32_e32 v12, 0x7f, v9
	s_waitcnt lgkmcnt(0)
	v_ashrrev_i32_e32 v11, 31, v10
	v_and_b32_e32 v13, 0x7fffffff, v11
	v_bitop3_b32 v11, v11, v10, s3 bitop3:0x6c
	v_lshlrev_b32_e32 v14, 2, v11
	v_and_b32_e32 v14, 16, v14
	s_lshl_b32 s3, s20, 7
	v_bitop3_b32 v13, v13, s6, v10 bitop3:0x48
	v_or3_b32 v13, v13, s3, v14
	v_bfrev_b32_e32 v14, 1
	v_cmp_lt_i32_e32 vcc, -1, v10
	v_lshrrev_b32_e32 v15, 1, v11
	v_and_b32_e32 v15, 12, v15
	v_cndmask_b32_e32 v10, -1, v14, vcc
	v_bitop3_b32 v11, v11, v10, s2 bitop3:0x6c
	s_movk_i32 s2, 0x3ff
	v_bitop3_b32 v10, v13, s2, v15 bitop3:0x36
	s_lshl_b32 s2, s22, 7
	s_addk_i32 s2, 0x80
	v_add_u32_e32 v9, s2, v9
	s_movk_i32 s2, 0x380
	v_and_or_b32 v9, v9, s2, v12
	v_lshlrev_b32_e32 v9, 3, v9
	global_atomic_umax_x2 v9, v[10:11], s[4:5]
	s_endpgm
